# v39 + QKV GEMM: first K-iteration runs a C=0 copy of the loop's first half, accumulator zero-fill removed
# speedup vs baseline: 1.0118x; 1.0039x over previous
; #define PG8_STAGEA(bufoff, gbase, h) do { if constexpr (GATHER) { PG8_STAGE(bufoff, gbase, vA[h]); } else { PG8_STAGE(bufoff, (gbase) + (h) * hstepA, voffA); } } while (0)
; #define PG8_LDA(dst, b, h) do { _Pragma("unroll") for (int m = 0; m < 4; ++m) _Pragma("unroll") for (int k = 0; k < 2; ++k) dst[m][k] = *(const LAS bf16x8*)(lds + PG8_SA(b, h) + aoff + m * 2048 + k * 1024); } while (0)
; #define PG8_MM(ai, bj, At, Bt) do { if constexpr (Epi::F8MMA) PG8_MMA8(ai, bj, At, Bt##8); else PG8_MMA(ai, bj, At, Bt); } while (0)
; #define PG8_WAIT_V(n) asm volatile("s_waitcnt vmcnt(" #n ")" ::: "memory")
; #define PG8_WAIT_L(n) asm volatile("s_waitcnt lgkmcnt(" #n ")" ::: "memory")
; #define PG8_BAR __builtin_amdgcn_s_barrier()
; #define PG8_SCHED __builtin_amdgcn_sched_barrier(0)
; template <class Epi, class Sched>
; __device__ __forceinline__ void gemm_phase(const int tid, LAS unsigned char* lds, const char* Abase, const int lda, const int ldb, const int K, const Sched& S, const Epi& E) {
;     ...
;             PG8_LDB(B0, 0, 0); PG8_LDB(B1, 0, 1); PG8_SCHED; PG8_LDA(At, 0, 0); PG8_STAGEA(PG8_SA(1, 1), a1, 1);
;             if constexpr (GATHER) { if (last) {
; #pragma unroll
;                 for (int h = 0; h < 2; ++h)
; #pragma unroll
;                     for (int i = 0; i < 2; ++i) vA[h][i] = vAn[h][i]; } }
;             PG8_WAIT_V(8); PG8_WAIT_L(0); PG8_BAR; PG8_MM(0, 0, At, B0); PG8_MM(0, 1, At, B1); PG8_BAR; PG8_SCHED;
;             PG8_LDA(At, 0, 1); PG8_STAGE(PG8_SB(0, 0), b2, voffB); PG8_STAGE(PG8_SB(0, 1), b2 + hstepB, voffB); PG8_STAGEA(PG8_SA(0, 0), a2, 0);
;             PG8_WAIT_V(8); PG8_WAIT_L(0); PG8_BAR; PG8_MM(1, 0, At, B0); PG8_MM(1, 1, At, B1); PG8_BAR; PG8_SCHED;
.LBB0_206:
	s_andn2_b64 vcc, exec, s[44:45]
	s_cbranch_vccnz .LBB0_217
	s_ashr_i32 s2, s73, 2
	s_mul_i32 s2, s2, 0xaaaaaaab
	s_add_i32 s2, s2, 0x2aaaaaaa
	s_cmp_lt_u32 s2, 0x55555555
	s_mov_b32 s2, 0x7a7a7a7a
	s_cselect_b32 s77, s2, 0x7b7b7b7b
	v_mov_b32_e32 v209, v3
	v_mov_b32_e32 v211, v3
	s_mov_b32 s78, 0
	s_mov_b64 s[2:3], 0x100
	s_waitcnt lgkmcnt(0)
	s_branch .LBB0_210
.Lpeel_qkv:
	s_add_i32 s78, s78, 2
	s_and_b64 s[54:55], s[56:57], exec
	s_cselect_b32 s55, 0, s2
	s_cselect_b32 s54, 0, s3
	s_add_u32 s62, s0, s55
	s_addc_u32 s63, s1, s54
	s_add_u32 s60, s52, s2
	s_addc_u32 s61, s53, s3
	s_add_u32 s54, s62, 0x80
	s_addc_u32 s55, s63, 0
	s_waitcnt vmcnt(8)
	s_and_b64 s[56:57], s[56:57], exec
	s_waitcnt lgkmcnt(0)
	s_cselect_b32 s56, s50, s60
	s_cselect_b32 s57, s51, s61
	s_add_u32 s60, s56, 0x80
	s_addc_u32 s61, s57, 0
	s_barrier
	s_setprio 1
	v_mov_b32_e32 v205, s77
	s_waitcnt lgkmcnt(0)
	s_nop 0
	v_mfma_scale_f32_16x16x128_f8f6f4 v[192:195], v[20:27], v[60:67], 0, v205, v216 op_sel_hi:[0,0,0]
	v_mfma_scale_f32_16x16x128_f8f6f4 v[188:191], v[28:35], v[60:67], 0, v205, v216 op_sel_hi:[0,0,0]
	v_mfma_scale_f32_16x16x128_f8f6f4 v[176:179], v[20:27], v[52:59], 0, v205, v216 op_sel_hi:[0,0,0]
	v_mfma_scale_f32_16x16x128_f8f6f4 v[172:175], v[28:35], v[52:59], 0, v205, v216 op_sel_hi:[0,0,0]
	v_mfma_scale_f32_16x16x128_f8f6f4 v[160:163], v[20:27], v[44:51], 0, v205, v216 op_sel_hi:[0,0,0]
	v_mfma_scale_f32_16x16x128_f8f6f4 v[156:159], v[28:35], v[44:51], 0, v205, v216 op_sel_hi:[0,0,0]
	v_mfma_scale_f32_16x16x128_f8f6f4 v[144:147], v[20:27], v[36:43], 0, v205, v216 op_sel_hi:[0,0,0]
	v_mfma_scale_f32_16x16x128_f8f6f4 v[140:143], v[28:35], v[36:43], 0, v205, v216 op_sel_hi:[0,0,0]
	s_setprio 0
	s_setprio 1
	v_mfma_scale_f32_16x16x128_f8f6f4 v[184:187], v[4:11], v[60:67], 0, v205, v216 op_sel_hi:[0,0,0]
	v_mfma_scale_f32_16x16x128_f8f6f4 v[180:183], v[12:19], v[60:67], 0, v205, v216 op_sel_hi:[0,0,0]
	v_mfma_scale_f32_16x16x128_f8f6f4 v[168:171], v[4:11], v[52:59], 0, v205, v216 op_sel_hi:[0,0,0]
	v_mfma_scale_f32_16x16x128_f8f6f4 v[164:167], v[12:19], v[52:59], 0, v205, v216 op_sel_hi:[0,0,0]
	v_mfma_scale_f32_16x16x128_f8f6f4 v[152:155], v[4:11], v[44:51], 0, v205, v216 op_sel_hi:[0,0,0]
	v_mfma_scale_f32_16x16x128_f8f6f4 v[148:151], v[12:19], v[44:51], 0, v205, v216 op_sel_hi:[0,0,0]
	v_mfma_scale_f32_16x16x128_f8f6f4 v[136:139], v[4:11], v[36:43], 0, v205, v216 op_sel_hi:[0,0,0]
	v_mfma_scale_f32_16x16x128_f8f6f4 v[132:135], v[12:19], v[36:43], 0, v205, v216 op_sel_hi:[0,0,0]
	s_setprio 0
	s_barrier
	s_mov_b32 m0, s10
	v_lshl_add_u64 v[228:229], s[56:57], 0, v[198:199]
	s_add_u32 s82, s56, 0x8000
	ds_read_b128 v[36:39], v245 offset:16384
	ds_read_b128 v[40:43], v245 offset:17408
	ds_read_b128 v[44:47], v245 offset:18432
	ds_read_b128 v[48:51], v245 offset:19456
	ds_read_b128 v[52:55], v245 offset:20480
	ds_read_b128 v[56:59], v245 offset:21504
	ds_read_b128 v[60:63], v245 offset:22528
	ds_read_b128 v[64:67], v245 offset:23552
	global_load_lds_dwordx4 v[228:229], off
	v_lshl_add_u64 v[228:229], s[56:57], 0, v[196:197]
	s_mov_b32 m0, s11
	s_addc_u32 s83, s57, 0
	global_load_lds_dwordx4 v[228:229], off
	v_lshl_add_u64 v[228:229], s[82:83], 0, v[198:199]
	s_mov_b32 m0, s22
	s_nop 0
	global_load_lds_dwordx4 v[228:229], off
	v_lshl_add_u64 v[228:229], s[82:83], 0, v[196:197]
	s_mov_b32 m0, s25
	s_nop 0
	global_load_lds_dwordx4 v[228:229], off
	s_mov_b32 m0, s9
	s_nop 0
	global_load_lds_dwordx4 v200, s[62:63]
	s_mov_b32 m0, s28
	s_nop 0
	global_load_lds_dwordx4 v202, s[62:63]
	s_waitcnt vmcnt(8)
	s_waitcnt lgkmcnt(0)
	s_barrier
	s_setprio 1
	s_waitcnt lgkmcnt(0)
	v_mfma_scale_f32_16x16x128_f8f6f4 v[128:131], v[20:27], v[36:43], 0, v205, v216 op_sel_hi:[0,0,0]
	v_mfma_scale_f32_16x16x128_f8f6f4 v[124:127], v[28:35], v[36:43], 0, v205, v216 op_sel_hi:[0,0,0]
	v_mfma_scale_f32_16x16x128_f8f6f4 v[112:115], v[20:27], v[44:51], 0, v205, v216 op_sel_hi:[0,0,0]
	v_mfma_scale_f32_16x16x128_f8f6f4 v[108:111], v[28:35], v[44:51], 0, v205, v216 op_sel_hi:[0,0,0]
	v_mfma_scale_f32_16x16x128_f8f6f4 v[96:99], v[20:27], v[52:59], 0, v205, v216 op_sel_hi:[0,0,0]
	v_mfma_scale_f32_16x16x128_f8f6f4 v[92:95], v[28:35], v[52:59], 0, v205, v216 op_sel_hi:[0,0,0]
	v_mfma_scale_f32_16x16x128_f8f6f4 v[80:83], v[20:27], v[60:67], 0, v205, v216 op_sel_hi:[0,0,0]
	v_mfma_scale_f32_16x16x128_f8f6f4 v[76:79], v[28:35], v[60:67], 0, v205, v216 op_sel_hi:[0,0,0]
	s_setprio 0
	s_setprio 1
	v_mfma_scale_f32_16x16x128_f8f6f4 v[120:123], v[4:11], v[36:43], 0, v205, v216 op_sel_hi:[0,0,0]
	v_mfma_scale_f32_16x16x128_f8f6f4 v[116:119], v[12:19], v[36:43], 0, v205, v216 op_sel_hi:[0,0,0]
	v_mfma_scale_f32_16x16x128_f8f6f4 v[104:107], v[4:11], v[44:51], 0, v205, v216 op_sel_hi:[0,0,0]
	v_mfma_scale_f32_16x16x128_f8f6f4 v[100:103], v[12:19], v[44:51], 0, v205, v216 op_sel_hi:[0,0,0]
	v_mfma_scale_f32_16x16x128_f8f6f4 v[88:91], v[4:11], v[52:59], 0, v205, v216 op_sel_hi:[0,0,0]
	v_mfma_scale_f32_16x16x128_f8f6f4 v[84:87], v[12:19], v[52:59], 0, v205, v216 op_sel_hi:[0,0,0]
	v_mfma_scale_f32_16x16x128_f8f6f4 v[72:75], v[4:11], v[60:67], 0, v205, v216 op_sel_hi:[0,0,0]
	v_mfma_scale_f32_16x16x128_f8f6f4 v[68:71], v[12:19], v[60:67], 0, v205, v216 op_sel_hi:[0,0,0]
	s_setprio 0
	s_barrier
	s_branch .Lmid_qkv

; #define PG8_STAGEA(bufoff, gbase, h) do { if constexpr (GATHER) { PG8_STAGE(bufoff, gbase, vA[h]); } else { PG8_STAGE(bufoff, (gbase) + (h) * hstepA, voffA); } } while (0)
; #define PG8_LDA(dst, b, h) do { _Pragma("unroll") for (int m = 0; m < 4; ++m) _Pragma("unroll") for (int k = 0; k < 2; ++k) dst[m][k] = *(const LAS bf16x8*)(lds + PG8_SA(b, h) + aoff + m * 2048 + k * 1024); } while (0)
; #define PG8_MM(ai, bj, At, Bt) do { if constexpr (Epi::F8MMA) PG8_MMA8(ai, bj, At, Bt##8); else PG8_MMA(ai, bj, At, Bt); } while (0)
; #define PG8_WAIT_V(n) asm volatile("s_waitcnt vmcnt(" #n ")" ::: "memory")
; #define PG8_WAIT_L(n) asm volatile("s_waitcnt lgkmcnt(" #n ")" ::: "memory")
; #define PG8_BAR __builtin_amdgcn_s_barrier()
; #define PG8_SCHED __builtin_amdgcn_sched_barrier(0)
; template <class Epi, class Sched>
; __device__ __forceinline__ void gemm_phase(const int tid, LAS unsigned char* lds, const char* Abase, const int lda, const int ldb, const int K, const Sched& S, const Epi& E) {
;     ...
;             PG8_LDB(B0, 1, 0); PG8_LDB(B1, 1, 1); PG8_SCHED; PG8_LDA(At, 1, 0); PG8_STAGEA(PG8_SA(0, 1), a2, 1);
;             PG8_WAIT_V(8); PG8_WAIT_L(0); PG8_BAR; PG8_MM(0, 0, At, B0); PG8_MM(0, 1, At, B1); PG8_BAR; PG8_SCHED;
;             PG8_LDA(At, 1, 1); PG8_STAGE(PG8_SB(1, 0), b3, voffB); PG8_STAGE(PG8_SB(1, 1), b3 + hstepB, voffB); PG8_STAGEA(PG8_SA(1, 0), a3, 0);
;             PG8_WAIT_V(8); PG8_WAIT_L(0); PG8_BAR; PG8_MM(1, 0, At, B0); PG8_MM(1, 1, At, B1); PG8_BAR; PG8_SCHED;
;         }
.Lmid_qkv:
	s_add_i32 s79, 0, 0x18000
	s_add_i32 s82, 0, 0x1c000
	v_add_u32_e32 v16, s79, v201
	v_add_u32_e32 v32, s82, v201
	ds_read_b128 v[4:7], v16
	ds_read_b128 v[8:11], v16 offset:1024
	ds_read_b128 v[12:15], v16 offset:2048
	ds_read_b128 v[16:19], v16 offset:3072
	ds_read_b128 v[20:23], v32
	ds_read_b128 v[24:27], v32 offset:1024
	ds_read_b128 v[28:31], v32 offset:2048
	ds_read_b128 v[32:35], v32 offset:3072
	s_mov_b32 m0, s29
	v_lshl_add_u64 v[214:215], s[62:63], 0, v[214:215]
	ds_read_b128 v[36:39], v245 offset:32768
	ds_read_b128 v[40:43], v245 offset:33792
	ds_read_b128 v[44:47], v245 offset:34816
	ds_read_b128 v[48:51], v245 offset:35840
	ds_read_b128 v[52:55], v245 offset:36864
	ds_read_b128 v[56:59], v245 offset:37888
	ds_read_b128 v[60:63], v245 offset:38912
	ds_read_b128 v[64:67], v245 offset:39936
	global_load_lds_dwordx4 v[214:215], off
	v_lshl_add_u64 v[212:213], s[62:63], 0, v[212:213]
	s_mov_b32 m0, s64
	s_nop 0
	global_load_lds_dwordx4 v[212:213], off
	s_waitcnt vmcnt(8)
	s_waitcnt lgkmcnt(0)
	s_barrier
	s_setprio 1
	s_waitcnt lgkmcnt(0)
	v_mfma_scale_f32_16x16x128_f8f6f4 v[192:195], v[4:11], v[36:43], v[192:195], v205, v216 op_sel_hi:[0,0,0]
	v_mfma_scale_f32_16x16x128_f8f6f4 v[188:191], v[12:19], v[36:43], v[188:191], v205, v216 op_sel_hi:[0,0,0]
	v_mfma_scale_f32_16x16x128_f8f6f4 v[176:179], v[4:11], v[44:51], v[176:179], v205, v216 op_sel_hi:[0,0,0]
	v_mfma_scale_f32_16x16x128_f8f6f4 v[172:175], v[12:19], v[44:51], v[172:175], v205, v216 op_sel_hi:[0,0,0]
	v_mfma_scale_f32_16x16x128_f8f6f4 v[160:163], v[4:11], v[52:59], v[160:163], v205, v216 op_sel_hi:[0,0,0]
	v_mfma_scale_f32_16x16x128_f8f6f4 v[156:159], v[12:19], v[52:59], v[156:159], v205, v216 op_sel_hi:[0,0,0]
	v_mfma_scale_f32_16x16x128_f8f6f4 v[144:147], v[4:11], v[60:67], v[144:147], v205, v216 op_sel_hi:[0,0,0]
	v_mfma_scale_f32_16x16x128_f8f6f4 v[140:143], v[12:19], v[60:67], v[140:143], v205, v216 op_sel_hi:[0,0,0]
	s_setprio 0
	s_setprio 1
	v_mfma_scale_f32_16x16x128_f8f6f4 v[184:187], v[20:27], v[36:43], v[184:187], v205, v216 op_sel_hi:[0,0,0]
	v_mfma_scale_f32_16x16x128_f8f6f4 v[180:183], v[28:35], v[36:43], v[180:183], v205, v216 op_sel_hi:[0,0,0]
	v_mfma_scale_f32_16x16x128_f8f6f4 v[168:171], v[20:27], v[44:51], v[168:171], v205, v216 op_sel_hi:[0,0,0]
	v_mfma_scale_f32_16x16x128_f8f6f4 v[164:167], v[28:35], v[44:51], v[164:167], v205, v216 op_sel_hi:[0,0,0]
	v_mfma_scale_f32_16x16x128_f8f6f4 v[152:155], v[20:27], v[52:59], v[152:155], v205, v216 op_sel_hi:[0,0,0]
	v_mfma_scale_f32_16x16x128_f8f6f4 v[148:151], v[28:35], v[52:59], v[148:151], v205, v216 op_sel_hi:[0,0,0]
	v_mfma_scale_f32_16x16x128_f8f6f4 v[136:139], v[20:27], v[60:67], v[136:139], v205, v216 op_sel_hi:[0,0,0]
	v_mfma_scale_f32_16x16x128_f8f6f4 v[132:135], v[28:35], v[60:67], v[132:135], v205, v216 op_sel_hi:[0,0,0]
	s_setprio 0
	s_barrier
	s_add_i32 s62, s79, s8
	v_lshl_add_u64 v[212:213], s[60:61], 0, v[198:199]
	s_mov_b32 m0, s62
	ds_read_b128 v[36:39], v245 offset:49152
	ds_read_b128 v[40:43], v245 offset:50176
	ds_read_b128 v[44:47], v245 offset:51200
	ds_read_b128 v[48:51], v245 offset:52224
	ds_read_b128 v[52:55], v245 offset:53248
	ds_read_b128 v[56:59], v245 offset:54272
	ds_read_b128 v[60:63], v245 offset:55296
	ds_read_b128 v[64:67], v245 offset:56320
	global_load_lds_dwordx4 v[212:213], off
	s_add_i32 m0, s62, 0x2000
	s_add_u32 s56, s56, 0x8080
	v_lshl_add_u64 v[212:213], s[60:61], 0, v[196:197]
	s_addc_u32 s57, s57, 0
	s_add_i32 s60, s82, s8
	global_load_lds_dwordx4 v[212:213], off
	v_lshl_add_u64 v[212:213], s[56:57], 0, v[198:199]
	s_mov_b32 m0, s60
	s_nop 0
	global_load_lds_dwordx4 v[212:213], off
	v_lshl_add_u64 v[212:213], s[56:57], 0, v[196:197]
	s_add_i32 m0, s60, 0x2000
	s_nop 0
	global_load_lds_dwordx4 v[212:213], off
	s_mov_b32 m0, s65
	s_nop 0
	global_load_lds_dwordx4 v200, s[54:55]
	s_mov_b32 m0, s66
	s_nop 0
	global_load_lds_dwordx4 v202, s[54:55]
	s_waitcnt vmcnt(8)
	s_waitcnt lgkmcnt(0)
	s_barrier
	s_setprio 1
	s_waitcnt lgkmcnt(0)
	v_mfma_scale_f32_16x16x128_f8f6f4 v[128:131], v[4:11], v[36:43], v[128:131], v205, v216 op_sel_hi:[0,0,0]
	v_mfma_scale_f32_16x16x128_f8f6f4 v[124:127], v[12:19], v[36:43], v[124:127], v205, v216 op_sel_hi:[0,0,0]
	v_mfma_scale_f32_16x16x128_f8f6f4 v[112:115], v[4:11], v[44:51], v[112:115], v205, v216 op_sel_hi:[0,0,0]
	v_mfma_scale_f32_16x16x128_f8f6f4 v[108:111], v[12:19], v[44:51], v[108:111], v205, v216 op_sel_hi:[0,0,0]
	v_mfma_scale_f32_16x16x128_f8f6f4 v[96:99], v[4:11], v[52:59], v[96:99], v205, v216 op_sel_hi:[0,0,0]
	v_mfma_scale_f32_16x16x128_f8f6f4 v[92:95], v[12:19], v[52:59], v[92:95], v205, v216 op_sel_hi:[0,0,0]
	v_mfma_scale_f32_16x16x128_f8f6f4 v[80:83], v[4:11], v[60:67], v[80:83], v205, v216 op_sel_hi:[0,0,0]
	v_mfma_scale_f32_16x16x128_f8f6f4 v[76:79], v[12:19], v[60:67], v[76:79], v205, v216 op_sel_hi:[0,0,0]
	s_setprio 0
	s_setprio 1
	v_mfma_scale_f32_16x16x128_f8f6f4 v[120:123], v[20:27], v[36:43], v[120:123], v205, v216 op_sel_hi:[0,0,0]
	v_mfma_scale_f32_16x16x128_f8f6f4 v[116:119], v[28:35], v[36:43], v[116:119], v205, v216 op_sel_hi:[0,0,0]
	v_mfma_scale_f32_16x16x128_f8f6f4 v[104:107], v[20:27], v[44:51], v[104:107], v205, v216 op_sel_hi:[0,0,0]
	v_mfma_scale_f32_16x16x128_f8f6f4 v[100:103], v[28:35], v[44:51], v[100:103], v205, v216 op_sel_hi:[0,0,0]
	v_mfma_scale_f32_16x16x128_f8f6f4 v[88:91], v[20:27], v[52:59], v[88:91], v205, v216 op_sel_hi:[0,0,0]
	v_mfma_scale_f32_16x16x128_f8f6f4 v[84:87], v[28:35], v[52:59], v[84:87], v205, v216 op_sel_hi:[0,0,0]
	v_mfma_scale_f32_16x16x128_f8f6f4 v[72:75], v[20:27], v[60:67], v[72:75], v205, v216 op_sel_hi:[0,0,0]
	v_mfma_scale_f32_16x16x128_f8f6f4 v[68:71], v[28:35], v[60:67], v[68:71], v205, v216 op_sel_hi:[0,0,0]
	s_setprio 0
	s_barrier
	s_add_u32 s2, s2, 0x100
	s_addc_u32 s3, s3, 0
	s_cmp_ge_i32 s78, s5
	s_cbranch_scc1 .LBB0_212
; #define PG8_STAGEA(bufoff, gbase, h) do { if constexpr (GATHER) { PG8_STAGE(bufoff, gbase, vA[h]); } else { PG8_STAGE(bufoff, (gbase) + (h) * hstepA, voffA); } } while (0)
; #define PG8_LDA(dst, b, h) do { _Pragma("unroll") for (int m = 0; m < 4; ++m) _Pragma("unroll") for (int k = 0; k < 2; ++k) dst[m][k] = *(const LAS bf16x8*)(lds + PG8_SA(b, h) + aoff + m * 2048 + k * 1024); } while (0)
; #define PG8_SCHED __builtin_amdgcn_sched_barrier(0)
; template <class Epi, class Sched>
; __device__ __forceinline__ void gemm_phase(const int tid, LAS unsigned char* lds, const char* Abase, const int lda, const int ldb, const int K, const Sched& S, const Epi& E) {
;     ...
;         for (int t = 0; t < nt; t += 2) {
;             const bool last = (t == nt - 2);
;             const char* a1 = cA + (size_t)(t + 1) * kstepA;
;             const char* a2 = last ? nA : cA + (size_t)(t + 2) * kstepA; const char* b2 = last ? nB : cB + (size_t)(t + 2) * kstep;
;             const char* a3 = a2 + kstepA; const char* b3 = b2 + kstep;
;             PG8_LDB(B0, 0, 0); PG8_LDB(B1, 0, 1); PG8_SCHED; PG8_LDA(At, 0, 0); PG8_STAGEA(PG8_SA(1, 1), a1, 1);
.LBB0_210:
	v_add_u32_e32 v4, 0, v201
	v_add_u32_e32 v5, 0x10000, v4
	v_add_u32_e32 v16, 0x14000, v4
	ds_read_b128 v[20:23], v5
	ds_read_b128 v[24:27], v5 offset:1024
	ds_read_b128 v[28:31], v5 offset:2048
	ds_read_b128 v[32:35], v5 offset:3072
	ds_read_b128 v[4:7], v16
	ds_read_b128 v[8:11], v16 offset:1024
	ds_read_b128 v[12:15], v16 offset:2048
	ds_read_b128 v[16:19], v16 offset:3072
	s_cmp_eq_u32 s68, s78
	s_cselect_b64 s[56:57], -1, 0
	s_add_u32 s54, s0, s2
	s_addc_u32 s55, s1, s3
	s_add_u32 s54, s54, 0xffffff80
	s_addc_u32 s55, s55, -1
	s_add_i32 m0, s9, 0xc000
	s_add_i32 s60, s9, 0xe000
	s_cmp_lg_u32 s68, s78
	ds_read_b128 v[60:63], v245
	ds_read_b128 v[64:67], v245 offset:1024
	ds_read_b128 v[52:55], v245 offset:2048
	ds_read_b128 v[56:59], v245 offset:3072
	ds_read_b128 v[44:47], v245 offset:4096
	ds_read_b128 v[48:51], v245 offset:5120
	ds_read_b128 v[36:39], v245 offset:6144
	ds_read_b128 v[40:43], v245 offset:7168
	global_load_lds_dwordx4 v2, s[54:55]
	s_mov_b32 m0, s60
	s_nop 0
	global_load_lds_dwordx4 v204, s[54:55]
	s_cbranch_scc0 .LBB0_208
	v_mov_b32_e32 v205, v3
	v_mov_b64_e32 v[212:213], v[204:205]
	v_mov_b64_e32 v[214:215], v[2:3]
	s_cmp_eq_u32 s78, 0
	s_cbranch_scc1 .Lpeel_qkv
	s_branch .LBB0_209
